# speedup vs baseline: 1.0652x; 1.0015x over previous
.LBB1_6:
	s_or_b64 exec, exec, s[12:13]
	s_load_dwordx4 s[36:39], s[0:1], 0x38
	s_add_i32 s0, 0, 0x23000
	v_lshl_add_u32 v222, v0, 2, s0
	v_readfirstlane_b32 s0, v0
	s_lshl_b32 s12, s0, 4
	s_and_b32 s0, s12, 0xfffffc00
	s_add_i32 s3, 0, 0x8000
	s_cmp_lg_u32 s3, -1
	s_cselect_b32 s1, s3, 0
	s_add_i32 s14, s0, s1
	s_add_u32 s0, s44, 0x2000
	v_mov_b32_e32 v2, 0x3c00
	v_cmp_eq_u32_e32 vcc, v221, v217
	v_or_b32_e32 v5, 1, v217
	v_lshlrev_b32_e32 v226, 4, v0
	s_mov_b32 m0, s14
	s_nop 0
	global_load_lds_dwordx4 v226, s[44:45]
	s_addc_u32 s1, s45, 0
	s_add_i32 s15, s14, 0x2000
	v_cndmask_b32_e32 v3, 0, v2, vcc
	v_or_b32_e32 v4, 2, v217
	v_cmp_eq_u32_e32 vcc, v221, v5
	s_mov_b32 m0, s15
	s_nop 0
	global_load_lds_dwordx4 v226, s[0:1]
	s_add_u32 s0, s44, 0x4000
	v_or_b32_e32 v7, 3, v217
	v_cndmask_b32_e32 v5, 0, v2, vcc
	v_cmp_eq_u32_e32 vcc, v221, v4
	s_addc_u32 s1, s45, 0
	s_add_i32 s15, s14, 0x4000
	v_cndmask_b32_e32 v4, 0, v2, vcc
	v_or_b32_e32 v6, 8, v217
	v_cmp_eq_u32_e32 vcc, v221, v7
	s_mov_b32 m0, s15
	s_nop 0
	global_load_lds_dwordx4 v226, s[0:1]
	s_add_u32 s0, s44, 0x6000
	v_or_b32_e32 v8, 10, v217
	v_cndmask_b32_e32 v7, 0, v2, vcc
	v_cmp_eq_u32_e32 vcc, v221, v6
	s_addc_u32 s1, s45, 0
	s_add_i32 s15, s14, 0x6000
	v_cndmask_b32_e32 v6, 0, v2, vcc
	v_or_b32_e32 v9, 9, v217
	v_cmp_eq_u32_e32 vcc, v221, v8
	s_mov_b32 m0, s15
	s_nop 0
	global_load_lds_dwordx4 v226, s[0:1]
	s_add_u32 s0, s44, 0x8000
	v_or_b32_e32 v10, 11, v217
	v_cndmask_b32_e32 v8, 0, v2, vcc
	v_cmp_eq_u32_e32 vcc, v221, v9
	s_addc_u32 s1, s45, 0
	s_and_b32 s12, s12, 0xfffff000
	v_cndmask_b32_e32 v9, 0, v2, vcc
	v_cmp_eq_u32_e32 vcc, v221, v10
	v_pack_b32_f16 v178, v3, v5
	v_or_b32_e32 v3, 16, v217
	s_sub_i32 s15, s14, s12
	v_cndmask_b32_e32 v10, 0, v2, vcc
	v_cmp_eq_u32_e32 vcc, v221, v3
	v_or_b32_e32 v5, 17, v217
	s_add_i32 s15, s15, 0x8000
	v_pack_b32_f16 v179, v4, v7
	v_cndmask_b32_e32 v3, 0, v2, vcc
	v_or_b32_e32 v4, 18, v217
	v_cmp_eq_u32_e32 vcc, v221, v5
	v_and_b32_e32 v224, 0xff0, v226
	s_mov_b32 m0, s15
	s_nop 0
	global_load_lds_dwordx4 v224, s[0:1]
	s_add_u32 s0, s44, 0x9000
	v_cndmask_b32_e32 v5, 0, v2, vcc
	v_cmp_eq_u32_e32 vcc, v221, v4
	v_or_b32_e32 v7, 19, v217
	s_addc_u32 s1, s45, 0
	s_add_i32 s15, s14, 0x9000
	v_pack_b32_f16 v180, v6, v9
	v_cndmask_b32_e32 v4, 0, v2, vcc
	v_or_b32_e32 v6, 24, v217
	v_cmp_eq_u32_e32 vcc, v221, v7
	s_mov_b32 m0, s15
	s_nop 0
	global_load_lds_dwordx4 v226, s[0:1]
	s_add_u32 s0, s44, 0xb000
	v_pack_b32_f16 v181, v8, v10
	v_cndmask_b32_e32 v7, 0, v2, vcc
	v_cmp_eq_u32_e32 vcc, v221, v6
	v_or_b32_e32 v8, 26, v217
	s_addc_u32 s1, s45, 0
	s_add_i32 s16, s14, 0xb000
	v_cndmask_b32_e32 v6, 0, v2, vcc
	v_or_b32_e32 v9, 25, v217
	v_cmp_eq_u32_e32 vcc, v221, v8
	s_mov_b32 m0, s16
	s_nop 0
	global_load_lds_dwordx4 v226, s[0:1]
	s_add_u32 s0, s44, 0xd000
	v_or_b32_e32 v10, 27, v217
	v_cndmask_b32_e32 v8, 0, v2, vcc
	v_cmp_eq_u32_e32 vcc, v221, v9
	s_addc_u32 s1, s45, 0
	s_add_i32 s16, s14, 0xd000
	v_cndmask_b32_e32 v9, 0, v2, vcc
	v_cmp_eq_u32_e32 vcc, v221, v10
	s_mov_b32 m0, s16
	s_nop 0
	global_load_lds_dwordx4 v226, s[0:1]
	s_add_u32 s0, s44, 0xf000
	s_addc_u32 s1, s45, 0
	v_cndmask_b32_e32 v2, 0, v2, vcc
	s_add_i32 s14, s14, 0xf000
	v_pack_b32_f16 v185, v8, v2
	v_mbcnt_lo_u32_b32 v2, -1, 0
	s_mov_b32 m0, s14
	s_nop 0
	global_load_lds_dwordx4 v226, s[0:1]
	s_add_u32 s0, s44, 0x11000
	v_mbcnt_hi_u32_b32 v2, -1, v2
	s_addc_u32 s1, s45, 0
	s_sub_i32 s12, s15, s12
	v_pack_b32_f16 v183, v4, v7
	v_and_b32_e32 v4, 64, v2
	s_add_i32 s12, s12, 0x8000
	s_mov_b32 m0, s12
	s_nop 0
	global_load_lds_dwordx4 v224, s[0:1]
	v_pack_b32_f16 v182, v3, v5
	v_xor_b32_e32 v3, 32, v2
	v_add_u32_e32 v4, 64, v4
	s_waitcnt vmcnt(0)
	v_cmp_lt_i32_e32 vcc, v3, v4
	s_mov_b32 s13, 0
	v_pack_b32_f16 v184, v6, v9
	v_cndmask_b32_e32 v2, v2, v3, vcc
	v_lshlrev_b32_e32 v225, 2, v2
	v_cmp_gt_u32_e64 s[0:1], 32, v216
	v_lshlrev_b32_e32 v227, 10, v220
	v_lshlrev_b32_e32 v207, 7, v220
	v_lshlrev_b32_e32 v246, 4, v207
	v_lshl_add_u32 v246, v1, 4, v246
	v_lshl_add_u32 v247, v227, 4, v206
	s_mov_b64 s[14:15], -1
	s_mov_b32 s49, 0x2da000
	s_mov_b32 s52, 0x2db000
	s_xor_b64 s[46:47], s[4:5], -1
	s_movk_i32 s53, 0x3844
	s_movk_i32 s54, 0x2bdb
	s_mov_b32 s55, 0xb160
	s_movk_i32 s56, 0x34e2
	s_mov_b32 s57, 0xad10
	s_mov_b32 s58, 0xb1ec
	s_movk_i32 s59, 0x31f0
	s_mov_b32 s60, 0xab4a
	s_brev_b32 s48, 60
	s_mov_b32 s61, 0x800000
	v_mov_b32_e32 v186, 0x43804380
	v_mov_b32_e32 v187, 0
	v_mov_b32_e32 v188, 0xac0d
	s_mov_b32 s62, 0
	s_mov_b32 s33, 0
	s_waitcnt lgkmcnt(0)
	s_barrier
	s_cmp_lg_u32 s4, 0
	s_cbranch_scc0 .Lprio_skip
	s_setprio 1
.Lprio_skip:
	s_branch .LBB1_8
.LBB1_7:
	s_or_b64 exec, exec, s[14:15]
	s_mov_b32 s62, 1
	s_mov_b64 s[14:15], 0
	s_and_b64 vcc, exec, s[50:51]
	s_cbranch_vccnz .LBB1_23
